# drain uses early s_part read + fused-DPP merge; dead shuffle-index setup and one same-wave barrier removed from the recheck
# baseline (speedup 1.0000x reference)
.LBB0_97:
	v_add_u32_e32 v254, 0x1200, v185
	ds_read_b128 v[250:253], v254
	v_cmp_lt_i32_e64 s[0:1], -1, v192
	s_waitcnt vmcnt(0)
	s_and_saveexec_b64 s[6:7], s[0:1]
	s_cbranch_execz .Low_a_doned
	v_pk_add_f32 v[66:67], v[246:247], v[224:225] neg_lo:[0,1] neg_hi:[0,1]
	v_pk_add_f32 v[74:75], v[248:249], v[226:227] neg_lo:[0,1] neg_hi:[0,1]
	v_pk_fma_f32 v[222:223], v[66:67], v[66:67], v[222:223]
	v_pk_fma_f32 v[222:223], v[74:75], v[74:75], v[222:223]
	v_pk_add_f32 v[66:67], v[224:225], v[66:67]
	v_pk_add_f32 v[68:69], v[226:227], v[74:75]
	global_store_dwordx4 v[168:169], v[66:69], off sc0 sc1
	s_nop 1

.Low_b_doned:
	s_or_b64 exec, exec, s[6:7]
	v_add_f32_e32 v167, v167, v222
	v_add_f32_e32 v167, v167, v223
	s_waitcnt lgkmcnt(0)
	v_lshlrev_b32_e32 v210, 1, v250
	v_lshlrev_b32_e32 v211, 1, v252
	v_and_b32_e32 v212, 0xfffffc03, v250
	v_and_b32_e32 v213, 0xfffffc03, v252
	v_and_b32_e32 v210, 0x78, v210
	v_and_b32_e32 v211, 0x78, v211
	v_or3_b32 v212, v212, v210, v176
	v_or3_b32 v213, v213, v211, v187
	v_min_f32_e32 v210, v212, v213
	v_max_f32_e32 v211, v212, v213
	v_min3_f32 v211, v251, v253, v211
	v_max_f32_dpp v212, v210, v210 quad_perm:[1,0,3,2] row_mask:0xf bank_mask:0xf
	v_min_f32_dpp v213, v210, v210 quad_perm:[1,0,3,2] row_mask:0xf bank_mask:0xf
	v_mov_b32_dpp v254, v211 quad_perm:[1,0,3,2] row_mask:0xf bank_mask:0xf
	v_min3_f32 v211, v211, v254, v212
	v_max_f32_dpp v212, v213, v213 quad_perm:[2,3,0,1] row_mask:0xf bank_mask:0xf
	v_min_f32_dpp v210, v213, v213 quad_perm:[2,3,0,1] row_mask:0xf bank_mask:0xf
	v_mov_b32_dpp v254, v211 quad_perm:[2,3,0,1] row_mask:0xf bank_mask:0xf
	v_min3_f32 v211, v211, v254, v212
	v_max_f32_dpp v212, v210, v210 row_half_mirror row_mask:0xf bank_mask:0xf
	v_min_f32_dpp v213, v210, v210 row_half_mirror row_mask:0xf bank_mask:0xf
	v_mov_b32_dpp v254, v211 row_half_mirror row_mask:0xf bank_mask:0xf
	v_min3_f32 v211, v211, v254, v212
	s_and_saveexec_b64 s[6:7], vcc
	s_cbranch_execz .Low_m_doned
	v_sub_f32_e32 v212, v211, v213
	v_cmp_gt_f32_e64 s[0:1], s26, v212
	s_nop 1
	v_cndmask_b32_e64 v212, 0, v190, s[0:1]
	v_and_or_b32 v212, v213, s27, v212
	ds_write_b32 v186, v212
	s_and_b64 exec, exec, s[0:1]
	s_cbranch_execz .Low_m_doned
	s_mov_b64 s[14:15], exec
	v_mbcnt_lo_u32_b32 v212, s14, 0
	v_mbcnt_hi_u32_b32 v212, s15, v212
	v_cmp_eq_u32_e64 s[0:1], 0, v212
	s_and_saveexec_b64 s[8:9], s[0:1]
	s_bcnt1_i32_b64 s0, s[14:15]
	v_mov_b32_e32 v254, s0
	ds_add_rtn_u32 v254, v189, v254
	s_or_b64 exec, exec, s[8:9]
	s_waitcnt lgkmcnt(0)
	v_readfirstlane_b32 s0, v254
	v_add_f32_e32 v213, 0x3d4ccccd, v213
	s_nop 0
	v_add_lshl_u32 v212, s0, v212, 2
	v_add_u32_e32 v254, 0x21400, v212
	v_add_u32_e32 v212, 0x20400, v212
	ds_write_b32 v254, v166
	ds_write_b32 v212, v213

.LBB0_102:
	v_lshlrev_b32_e32 v71, 2, v183
	s_waitcnt lgkmcnt(0)
	v_or_b32_e32 v66, 0x213c0, v71
	ds_read_b32 v70, v66
	v_or_b32_e32 v71, 0x21380, v71
	s_movk_i32 s4, 0x3ff0
	ds_read_b32 v71, v71
	s_waitcnt lgkmcnt(1)
	v_lshlrev_b32_e32 v66, 4, v70
	v_and_or_b32 v66, v66, s4, v1
	v_lshlrev_b32_e32 v66, 4, v66
	global_load_dwordx4 v[66:69], v66, s[22:23]
	s_waitcnt lgkmcnt(0)
	v_cmp_lt_i32_e32 vcc, -1, v71
	s_and_saveexec_b64 s[0:1], vcc
	s_cbranch_execz .LBB0_104
	v_lshlrev_b32_e32 v71, 4, v71
	v_and_or_b32 v71, v71, s4, v1
	v_lshlrev_b32_e32 v71, 4, v71
	global_load_dwordx4 v[72:75], v71, s[22:23]
	ds_read_b128 v[76:79], v175 offset:24576
	v_or_b32_e32 v71, s24, v183
	s_mov_b32 s4, 0x1e000
	v_lshlrev_b32_e32 v71, 8, v71
	v_or3_b32 v71, v71, v178, s4
	s_waitcnt vmcnt(0) lgkmcnt(0)
	v_pk_add_f32 v[72:73], v[72:73], v[76:77] neg_lo:[0,1] neg_hi:[0,1]
	v_pk_add_f32 v[80:81], v[74:75], v[78:79] neg_lo:[0,1] neg_hi:[0,1]
	v_pk_mul_f32 v[82:83], v[72:73], v[72:73]
	v_pk_add_f32 v[72:73], v[76:77], v[72:73]
	v_pk_add_f32 v[74:75], v[78:79], v[80:81]
	v_pk_mul_f32 v[76:77], v[80:81], v[80:81]
	global_store_dwordx4 v71, v[72:75], s[12:13] sc0 sc1
	v_add_f32_e32 v71, v82, v83
	v_add_f32_e32 v71, v71, v76
	v_add_f32_e32 v71, v71, v77
	v_add_f32_e32 v167, v167, v71

.Lcx_doneb:
	s_waitcnt lgkmcnt(0)
	s_barrier
	ds_read_b32 v66, v248
	s_waitcnt lgkmcnt(0)
	v_cmp_ne_u32_e32 vcc, 0, v66
	s_cbranch_vccz .LBB0_447
	v_min_u32_e32 v70, 0x800, v66
	s_lshl_b32 s14, s25, 2
	s_add_i32 s14, s14, 0x21400
	s_mov_b32 s15, 0
	v_mov_b32_e32 v75, v247
	s_branch .LBB0_443

.LBB0_451:
	s_or_b64 exec, exec, s[0:1]
	s_and_b64 s[8:9], s[6:7], s[8:9]
	s_and_saveexec_b64 s[0:1], s[8:9]
	s_cbranch_execz .LBB0_109
	v_lshl_add_u32 v67, v253, 2, v252
	ds_write_b32 v67, v66
	s_branch .LBB0_109
